# exp1 chunk preamble: chained tilee/tokof global loads (5 x load->vmcnt(0)) replaced by the lane table and the LDS row table built at chunk entry
# speedup vs baseline: 1.0146x; 1.0024x over previous
.LBB0_3477:
	s_andn2_b64 vcc, exec, s[14:15]
	s_cbranch_vccnz .LBB0_3471
	v_bfe_i32 v5, v2, 27, 1
	v_lshlrev_b32_e32 v3, 4, v2
	v_lshrrev_b32_e32 v5, 22, v5
	v_add_u32_e32 v5, v3, v5
	v_and_b32_e32 v5, 0xfffffc00, v5
	v_ashrrev_i32_e32 v4, 31, v2
	v_sub_u32_e32 v5, v3, v5
	v_lshrrev_b32_e32 v4, 26, v4
	v_lshrrev_b32_e32 v6, 4, v5
	v_add_u32_e32 v4, v2, v4
	v_bitop3_b32 v6, v6, v5, 32 bitop3:0x6c
	v_ashrrev_i32_e32 v5, 31, v5
	v_ashrrev_i32_e32 v4, 6, v4
	v_lshrrev_b32_e32 v5, 26, v5
	v_lshlrev_b32_e32 v7, 3, v4
	v_add_u32_e32 v5, v6, v5
	v_and_b32_e32 v7, -16, v7
	v_ashrrev_i32_e32 v5, 6, v5
	v_add_u32_e32 v188, v5, v7
	v_mul_i32_i24_e32 v7, 64, v5
	v_sub_u32_e32 v6, v6, v7
	v_lshlrev_b32_e32 v4, 5, v4
	v_ashrrev_i16_sdwa v6, v211, sext(v6) dst_sel:DWORD dst_unused:UNUSED_PAD src0_sel:DWORD src1_sel:BYTE_0
	v_and_b32_e32 v4, 32, v4
	v_bfe_i32 v6, v6, 0, 16
	v_add_u32_e32 v3, 0x2000, v3
	v_add_lshl_u32 v189, v4, v6, 1
	v_ashrrev_i32_e32 v4, 31, v3
	v_lshlrev_b32_e32 v7, 1, v188
	v_lshrrev_b32_e32 v8, 2, v188
	v_and_b32_e32 v5, 3, v5
	s_mov_b32 s12, 0x1fffe0
	v_lshrrev_b32_e32 v4, 22, v4
	v_and_b32_e32 v7, 24, v7
	v_and_b32_e32 v8, 4, v8
	v_and_or_b32 v5, v188, s12, v5
	v_add_u32_e32 v4, v3, v4
	v_or3_b32 v5, v5, v8, v7
	v_ashrrev_i32_e32 v4, 10, v4
	v_lshl_add_u32 v164, v5, 11, v189
	v_mul_i32_i24_e32 v5, 0x400, v4
	v_sub_u32_e32 v3, v3, v5
	v_lshrrev_b32_e32 v5, 4, v3
	v_bitop3_b32 v3, v5, v3, 32 bitop3:0x6c
	v_ashrrev_i32_e32 v6, 31, v3
	v_lshrrev_b32_e32 v6, 26, v6
	v_lshlrev_b32_e32 v5, 3, v4
	v_add_u32_e32 v6, v3, v6
	v_and_b32_e32 v5, -16, v5
	v_ashrrev_i32_e32 v7, 6, v6
	v_add_u32_e32 v190, v7, v5
	v_and_b32_e32 v5, 0xc0, v6
	s_ashr_i32 s18, s31, 6
	s_ashr_i32 s21, s20, 31
	s_ashr_i32 s4, s31, 8
	v_sub_u32_e32 v3, v3, v5
	s_lshl_b32 s34, s18, 10
	s_lshl_b64 s[14:15], s[20:21], 2
	v_lshlrev_b32_e32 v4, 5, v4
	v_ashrrev_i16_sdwa v3, v211, sext(v3) dst_sel:DWORD dst_unused:UNUSED_PAD src0_sel:DWORD src1_sel:BYTE_0
	s_add_u32 s14, s3, s14
	v_and_b32_e32 v4, 32, v4
	v_bfe_i32 v3, v3, 0, 16
	s_addc_u32 s15, s28, s15
	v_add_lshl_u32 v191, v4, v3, 1
	v_lshlrev_b32_e32 v5, 1, v190
	v_lshrrev_b32_e32 v6, 2, v190
	v_and_b32_e32 v7, 3, v7
	v_and_b32_e32 v5, 24, v5
	v_and_b32_e32 v6, 4, v6
	v_and_or_b32 v7, v190, s12, v7
	v_or3_b32 v5, v7, v6, v5
	v_lshl_add_u32 v166, v5, 11, v191
	v_readlane_b32 s14, v242, 0
	s_ashr_i32 s15, s14, 31
	s_lshl_b64 s[16:17], s[14:15], 21
	s_lshl_b32 s14, s5, 8
	s_ashr_i32 s15, s14, 31
	s_add_u32 s16, s49, s16
	s_addc_u32 s17, s50, s17
	s_lshl_b32 s19, s20, 8
	v_lshlrev_b32_e32 v4, 2, v188
	v_lshlrev_b32_e32 v5, 2, v190
	v_add_u32_e32 v4, 0x20000, v4
	v_add_u32_e32 v5, 0x20000, v5
	ds_read_b32 v168, v4
	ds_read_b32 v170, v5
	ds_read_b32 v172, v4 offset:512
	ds_read_b32 v174, v5 offset:512
	s_bitset1_b32 s19, 7
	s_lshl_b64 s[14:15], s[14:15], 11
	s_add_u32 s22, s16, s14
	s_addc_u32 s23, s17, s15
	s_add_i32 s21, s34, 0
	s_add_i32 m0, s21, 0x10000
	s_add_i32 s35, s21, 0x2000
	global_load_lds_dwordx4 v164, s[22:23]
	s_add_i32 m0, s21, 0x12000
	s_add_u32 s14, s22, 0x40000
	global_load_lds_dwordx4 v166, s[22:23]
	s_mov_b32 m0, s21
	s_addc_u32 s15, s23, 0
	s_add_i32 s41, s21, 0x4000
	s_add_i32 s43, s21, 0x6000
	s_waitcnt lgkmcnt(0)
	v_lshl_add_u32 v168, v168, 11, v189
	v_lshl_add_u32 v170, v170, 11, v191
	v_lshl_add_u32 v172, v172, 11, v189
	v_lshl_add_u32 v174, v174, 11, v191
	global_load_lds_dwordx4 v168, s[64:65]
	s_mov_b32 m0, s35
	s_nop 0
	global_load_lds_dwordx4 v170, s[64:65]
	s_add_i32 m0, s21, 0x14000
	s_nop 0
	s_nop 0
	s_nop 0
	s_nop 0
	s_nop 0
	s_nop 0
	s_nop 0
	s_nop 0
	s_nop 0
	s_nop 0
	s_nop 0
	s_nop 0
	s_nop 0
	s_nop 0
	global_load_lds_dwordx4 v164, s[14:15]
	s_add_i32 m0, s21, 0x16000
	s_cmp_lg_u32 s4, 1
	global_load_lds_dwordx4 v166, s[14:15]
	s_mov_b32 m0, s41
	s_nop 0
	global_load_lds_dwordx4 v172, s[64:65]
	s_mov_b32 m0, s43
	s_nop 0
	global_load_lds_dwordx4 v174, s[64:65]
	s_cbranch_scc1 .LBB0_3480
	s_barrier
